# baseline (speedup 1.0000x reference)
_Z6gemm_kILi1ELb1ELb0ELb1ELb1ELb0EEvPKtS1_ii7EpiArgs:
	s_load_dwordx4 s[4:7], s[0:1], 0x0
	v_readfirstlane_b32 s18, v0
	s_mov_b32 s69, 0
	s_cmp_lt_i32 s2, 12
	s_cbranch_scc0 .Lst_a_done
	s_cmp_lt_u32 s18, 0x100
	s_cbranch_scc0 .Lst_a_done
	s_mov_b32 s69, 1
	s_load_dwordx2 s[60:61], s[0:1], 0x28
	s_load_dwordx4 s[64:67], s[0:1], 0x38
	s_load_dwordx2 s[62:63], s[0:1], 0x50
	s_lshl_b32 s68, s2, 8
	v_or_b32_e32 v144, s68, v0
	v_lshlrev_b32_e32 v144, 2, v144
	s_waitcnt lgkmcnt(0)
	global_load_dword v117, v144, s[60:61]
	s_add_u32 s60, s60, 0x3000
	s_addc_u32 s61, s61, 0
	global_load_dword v118, v144, s[60:61]
	s_add_u32 s60, s60, 0x3000
	s_addc_u32 s61, s61, 0
	global_load_dword v119, v144, s[60:61]
	s_add_u32 s60, s60, 0x3000
	s_addc_u32 s61, s61, 0
	global_load_dword v120, v144, s[60:61]
	s_add_u32 s60, s60, 0x3000
	s_addc_u32 s61, s61, 0
	global_load_dword v121, v144, s[60:61]
	s_add_u32 s60, s60, 0x3000
	s_addc_u32 s61, s61, 0
	global_load_dword v122, v144, s[60:61]
	s_add_u32 s60, s60, 0x3000
	s_addc_u32 s61, s61, 0
	global_load_dword v123, v144, s[60:61]
	s_add_u32 s60, s60, 0x3000
	s_addc_u32 s61, s61, 0
	global_load_dword v124, v144, s[60:61]
	s_add_u32 s60, s60, 0x3000
	s_addc_u32 s61, s61, 0
	global_load_dword v125, v144, s[60:61]
	s_add_u32 s60, s60, 0x3000
	s_addc_u32 s61, s61, 0
	global_load_dword v126, v144, s[60:61]
	s_add_u32 s60, s60, 0x3000
	s_addc_u32 s61, s61, 0
	global_load_dword v127, v144, s[60:61]
	s_add_u32 s60, s60, 0x3000
	s_addc_u32 s61, s61, 0
	global_load_dword v128, v144, s[60:61]
	s_add_u32 s60, s60, 0x3000
	s_addc_u32 s61, s61, 0
	global_load_dword v129, v144, s[60:61]
	s_add_u32 s60, s60, 0x3000
	s_addc_u32 s61, s61, 0
	global_load_dword v130, v144, s[60:61]
	s_add_u32 s60, s60, 0x3000
	s_addc_u32 s61, s61, 0
	global_load_dword v131, v144, s[60:61]
	s_add_u32 s60, s60, 0x3000
	s_addc_u32 s61, s61, 0
	global_load_dword v132, v144, s[60:61]
	s_add_u32 s60, s60, 0x3000
	s_addc_u32 s61, s61, 0
	global_load_dword v133, v144, s[60:61]
	s_add_u32 s60, s60, 0x3000
	s_addc_u32 s61, s61, 0
	global_load_dword v134, v144, s[60:61]
	s_add_u32 s60, s60, 0x3000
	s_addc_u32 s61, s61, 0
	global_load_dword v135, v144, s[60:61]
	s_add_u32 s60, s60, 0x3000
	s_addc_u32 s61, s61, 0
	global_load_dword v136, v144, s[60:61]
	s_add_u32 s60, s60, 0x3000
	s_addc_u32 s61, s61, 0
	global_load_dword v137, v144, s[60:61]
	s_add_u32 s60, s60, 0x3000
	s_addc_u32 s61, s61, 0
	global_load_dword v138, v144, s[60:61]
	s_add_u32 s60, s60, 0x3000
	s_addc_u32 s61, s61, 0
	global_load_dword v139, v144, s[60:61]
	s_add_u32 s60, s60, 0x3000
	s_addc_u32 s61, s61, 0
	global_load_dword v140, v144, s[60:61]
	global_load_dword v141, v144, s[62:63]
.Lst_a_done:
	s_load_dwordx2 s[14:15], s[0:1], 0x30
	s_load_dwordx2 s[12:13], s[0:1], 0x48
	s_load_dwordx2 s[8:9], s[0:1], 0x10
	s_lshl_b32 s3, s2, 3
	s_and_b32 s3, s3, 56
	s_bfe_u32 s10, s2, 0x30003
	s_or_b32 s3, s3, s10
	s_lshl_b32 s3, s3, 7
	s_waitcnt lgkmcnt(0)
	s_mul_hi_i32 s21, s9, s3
	s_mul_i32 s20, s9, s3
	s_lshr_b32 s19, s18, 6
	s_bfe_u32 s24, s18, 0x20006
	s_ashr_i32 s2, s2, 6
	s_ashr_i32 s17, s9, 31
	s_lshl_b64 s[20:21], s[20:21], 1
	s_mul_i32 s10, s2, 0xc0
	s_add_u32 s4, s4, s20
	s_addc_u32 s5, s5, s21
	s_mul_hi_i32 s21, s9, s10
	s_mul_i32 s20, s9, s10
	s_ashr_i32 s11, s10, 31
	s_lshl_b64 s[20:21], s[20:21], 1
	s_add_u32 s6, s6, s20
	s_addc_u32 s7, s7, s21
	s_lshr_b32 s18, s18, 2
	v_lshrrev_b32_e32 v1, 4, v0
	s_lshl_b32 s26, s19, 10
	s_and_b32 s18, s18, 0x3fffffc0
	v_and_b32_e32 v2, 15, v0
	v_xor_b32_e32 v4, v1, v0
	v_bfe_u32 v5, v0, 1, 3
	s_cmp_lg_u32 0, -1
	v_lshrrev_b32_e32 v3, 3, v0
	v_lshlrev_b32_e32 v4, 3, v4
	s_mov_b32 s16, s9
	v_bitop3_b32 v5, v1, v5, 3 bitop3:0x6c
	v_or_b32_e32 v1, s18, v2
	s_cselect_b32 s18, 0, 0
	v_mul_lo_u32 v3, s9, v3
	v_and_b32_e32 v4, 56, v4
	s_add_i32 s26, s26, s18
	s_ashr_i32 s9, s9, 6
	s_lshl_b64 s[20:21], s[16:17], 7
	v_add_lshl_u32 v84, v3, v4, 1
	s_nop 4
	s_mov_b32 s18, m0
	s_mov_b32 m0, s26
	s_nop 0
	global_load_lds_dwordx4 v84, s[4:5]
	s_mov_b32 m0, s18
	s_add_u32 s16, s4, s20
	s_addc_u32 s17, s5, s21
	s_add_i32 s27, s26, 0x2000
	s_nop 4
	s_mov_b32 s18, m0
	s_mov_b32 m0, s27
	s_nop 0
	global_load_lds_dwordx4 v84, s[16:17]
	s_mov_b32 m0, s18
	s_add_i32 s28, s26, 0x4000
	s_nop 4
	s_mov_b32 s18, m0
	s_mov_b32 m0, s28
	s_nop 0
	global_load_lds_dwordx4 v84, s[6:7]
	s_mov_b32 m0, s18
	s_add_u32 s18, s6, s20
	s_addc_u32 s19, s7, s21
	s_add_i32 s29, s26, 0x6000
	s_nop 4
	s_mov_b32 s22, m0
	s_mov_b32 m0, s29
	s_nop 0
	global_load_lds_dwordx4 v84, s[18:19]
	s_mov_b32 m0, s22
	s_add_u32 s20, s18, s20
	s_addc_u32 s21, s19, s21
	s_add_i32 s30, s26, 0x8000
	s_nop 4
	s_mov_b32 s22, m0
	s_mov_b32 m0, s30
	s_nop 0
	global_load_lds_dwordx4 v84, s[20:21]
	s_mov_b32 m0, s22
	s_add_u32 s22, s4, 0x80
	s_addc_u32 s23, s5, 0
	s_add_i32 s31, s26, 0xa000
	s_nop 4
	s_mov_b32 s33, m0
	s_mov_b32 m0, s31
	s_nop 0
	global_load_lds_dwordx4 v84, s[22:23]
	s_mov_b32 m0, s33
	s_add_u32 s22, s16, 0x80
	s_addc_u32 s23, s17, 0
	s_add_i32 s33, s26, 0xc000
	s_nop 4
	s_mov_b32 s34, m0
	s_mov_b32 m0, s33
	s_nop 0
	global_load_lds_dwordx4 v84, s[22:23]
	s_mov_b32 m0, s34
	s_add_u32 s22, s6, 0x80
	s_addc_u32 s23, s7, 0
	s_add_i32 s34, s26, 0xe000
	s_nop 4
	s_mov_b32 s35, m0
	s_mov_b32 m0, s34
	s_nop 0
	global_load_lds_dwordx4 v84, s[22:23]
	s_mov_b32 m0, s35
	s_add_u32 s22, s18, 0x80
	s_addc_u32 s23, s19, 0
	s_add_i32 s35, s26, 0x10000
	s_nop 4
	s_mov_b32 s36, m0
	s_mov_b32 m0, s35
	s_nop 0
	global_load_lds_dwordx4 v84, s[22:23]
	s_mov_b32 m0, s36
	s_add_u32 s22, s20, 0x80
	s_addc_u32 s23, s21, 0
	s_add_i32 s36, s26, 0x12000
	s_nop 4
	s_mov_b32 s37, m0
	s_mov_b32 m0, s36
	s_nop 0
	global_load_lds_dwordx4 v84, s[22:23]
	s_mov_b32 m0, s37
	s_add_u32 s22, s4, 0x100
	s_addc_u32 s23, s5, 0
	s_add_i32 s37, s26, 0x14000
	s_nop 4
	s_mov_b32 s38, m0
	s_mov_b32 m0, s37
	s_nop 0
	global_load_lds_dwordx4 v84, s[22:23]
	s_mov_b32 m0, s38
	s_add_u32 s22, s16, 0x100
	s_addc_u32 s23, s17, 0
	s_add_i32 s38, s26, 0x16000
	s_nop 4
	s_mov_b32 s39, m0
	s_mov_b32 m0, s38
	s_nop 0
	global_load_lds_dwordx4 v84, s[22:23]
	s_mov_b32 m0, s39
	s_add_u32 s22, s6, 0x100
	s_addc_u32 s23, s7, 0
	s_add_i32 s39, s26, 0x18000
	s_nop 4
	s_mov_b32 s40, m0
	s_mov_b32 m0, s39
	s_nop 0
	global_load_lds_dwordx4 v84, s[22:23]
	s_mov_b32 m0, s40
	s_add_u32 s22, s18, 0x100
	s_mul_i32 s24, s24, 48
	s_addc_u32 s23, s19, 0
	s_add_i32 s40, s26, 0x1a000
	v_or_b32_e32 v2, s24, v2
	s_nop 4
	s_mov_b32 s41, m0
	s_mov_b32 m0, s40
	s_nop 0
	global_load_lds_dwordx4 v84, s[22:23]
	s_mov_b32 m0, s41
	s_add_u32 s22, s20, 0x100
	v_lshlrev_b32_e32 v5, 4, v5
	v_lshl_add_u32 v31, v2, 7, 0
	v_lshl_add_u32 v2, v1, 7, 0
	s_addc_u32 s23, s21, 0
	s_add_i32 s41, s26, 0x1c000
	s_nop 4
	s_mov_b32 s42, m0
	s_mov_b32 m0, s41
	s_nop 0
	global_load_lds_dwordx4 v84, s[22:23]
	s_mov_b32 m0, s42
	v_xor_b32_e32 v30, 64, v5
	v_add_u32_e32 v79, v2, v5
	s_waitcnt vmcnt(10) lgkmcnt(0)
	s_barrier
	s_cmp_lg_u32 s69, 0
	s_cbranch_scc0 .Lst_b_done
	v_add_f32_e32 v142, 0, v117
	v_add_f32_e32 v142, v142, v118
	v_add_f32_e32 v142, v142, v119
	v_add_f32_e32 v142, v142, v120
	v_add_f32_e32 v142, v142, v121
	v_add_f32_e32 v142, v142, v122
	v_add_f32_e32 v142, v142, v123
	v_add_f32_e32 v142, v142, v124
	v_add_f32_e32 v142, v142, v125
	v_add_f32_e32 v142, v142, v126
	v_add_f32_e32 v142, v142, v127
	v_add_f32_e32 v142, v142, v128
	v_add_f32_e32 v143, 0, v129
	v_add_f32_e32 v143, v143, v130
	v_add_f32_e32 v143, v143, v131
	v_add_f32_e32 v143, v143, v132
	v_add_f32_e32 v143, v143, v133
	v_add_f32_e32 v143, v143, v134
	v_add_f32_e32 v143, v143, v135
	v_add_f32_e32 v143, v143, v136
	v_add_f32_e32 v143, v143, v137
	v_add_f32_e32 v143, v143, v138
	v_add_f32_e32 v143, v143, v139
	v_add_f32_e32 v143, v143, v140
	v_add_f32_e32 v143, v143, v141
	global_store_dword v144, v142, s[64:65]
	global_store_dword v144, v143, s[66:67]
.Lst_b_done:
	v_add_u32_e32 v81, v31, v5
	v_add_u32_e32 v78, v2, v30
	ds_read_b128 v[22:25], v79 offset:2048
	ds_read_b128 v[18:21], v79 offset:4096
	ds_read_b128 v[2:5], v79 offset:6144
	ds_read_b128 v[10:13], v81 offset:16384
	ds_read_b128 v[14:17], v81 offset:18432
	ds_read_b128 v[26:29], v79
	ds_read_b128 v[6:9], v81 offset:20480
	v_add_u32_e32 v83, v31, v30
	s_mov_b32 s25, 3
	v_add_u32_e32 v80, 0x4000, v81
	v_add_u32_e32 v82, 0x4000, v83
	s_cmp_lt_i32 s9, 4
	v_mov_b32_e32 v65, 0
	s_cbranch_scc1 .LBB4_5
	v_mov_b32_e32 v66, 0
	v_add_u32_e32 v85, 0x14000, v79
	v_add_u32_e32 v86, 0x14000, v80
	v_add_u32_e32 v87, 0x14000, v78
	v_add_u32_e32 v88, 0x14000, v82
	v_add_u32_e32 v89, 0x14800, v79
	v_add_u32_e32 v90, 0x15000, v79
	v_add_u32_e32 v91, 0x15800, v79
	v_add_u32_e32 v92, 0x14800, v80
	v_add_u32_e32 v93, 0x15000, v80
	v_add_u32_e32 v94, 0x14800, v78
	v_add_u32_e32 v95, 0x15000, v78
	v_add_u32_e32 v96, 0x15800, v78
	v_add_u32_e32 v97, 0x14800, v82
	v_add_u32_e32 v98, 0x15000, v82
	s_mov_b64 s[22:23], 0
	v_mov_b32_e32 v67, v66
	v_mov_b32_e32 v68, v66
	v_mov_b32_e32 v69, v66
	v_mov_b32_e32 v58, v66
	v_mov_b32_e32 v59, v66
	v_mov_b32_e32 v60, v66
	v_mov_b32_e32 v61, v66
	v_mov_b32_e32 v50, v66
	v_mov_b32_e32 v51, v66
	v_mov_b32_e32 v52, v66
	v_mov_b32_e32 v53, v66
	v_mov_b32_e32 v34, v66
	v_mov_b32_e32 v35, v66
	v_mov_b32_e32 v36, v66
	v_mov_b32_e32 v37, v66
	v_mov_b32_e32 v42, v66
	v_mov_b32_e32 v43, v66
	v_mov_b32_e32 v44, v66
	v_mov_b32_e32 v45, v66
	v_mov_b32_e32 v46, v66
	v_mov_b32_e32 v47, v66
	v_mov_b32_e32 v48, v66
	v_mov_b32_e32 v49, v66
	v_mov_b32_e32 v30, v66
	v_mov_b32_e32 v31, v66
	v_mov_b32_e32 v32, v66
	v_mov_b32_e32 v33, v66
	v_mov_b32_e32 v38, v66
	v_mov_b32_e32 v39, v66
	v_mov_b32_e32 v40, v66
	v_mov_b32_e32 v41, v66
	v_mov_b32_e32 v54, v66
	v_mov_b32_e32 v55, v66
	v_mov_b32_e32 v56, v66
	v_mov_b32_e32 v57, v66
	v_mov_b32_e32 v70, v66
	v_mov_b32_e32 v71, v66
	v_mov_b32_e32 v72, v66
	v_mov_b32_e32 v73, v66
	v_mov_b32_e32 v74, v66
	v_mov_b32_e32 v75, v66
	v_mov_b32_e32 v76, v66
	v_mov_b32_e32 v77, v66
	v_mov_b32_e32 v62, v66
	v_mov_b32_e32 v63, v66
	v_mov_b32_e32 v64, v66
	v_mov_b32_e32 v65, v66

	.amdhsa_kernel _Z6gemm_kILi1ELb1ELb0ELb1ELb1ELb0EEvPKtS1_ii7EpiArgs
		.amdhsa_group_segment_fixed_size 0
		.amdhsa_private_segment_fixed_size 0
		.amdhsa_kernarg_size 88
		.amdhsa_user_sgpr_count 2
		.amdhsa_user_sgpr_dispatch_ptr 0
		.amdhsa_user_sgpr_queue_ptr 0
		.amdhsa_user_sgpr_kernarg_segment_ptr 1
		.amdhsa_user_sgpr_dispatch_id 0
		.amdhsa_user_sgpr_kernarg_preload_length 0
		.amdhsa_user_sgpr_kernarg_preload_offset 0
		.amdhsa_user_sgpr_private_segment_size 0
		.amdhsa_uses_dynamic_stack 0
		.amdhsa_enable_private_segment 0
		.amdhsa_system_sgpr_workgroup_id_x 1
		.amdhsa_system_sgpr_workgroup_id_y 0
		.amdhsa_system_sgpr_workgroup_id_z 0
		.amdhsa_system_sgpr_workgroup_info 0
		.amdhsa_system_vgpr_workitem_id 0
		.amdhsa_next_free_vgpr 145
		.amdhsa_next_free_sgpr 70
		.amdhsa_accum_offset 148
		.amdhsa_reserve_vcc 1
		.amdhsa_float_round_mode_32 0
		.amdhsa_float_round_mode_16_64 0
		.amdhsa_float_denorm_mode_32 3
		.amdhsa_float_denorm_mode_16_64 3
		.amdhsa_dx10_clamp 1
		.amdhsa_ieee_mode 1
		.amdhsa_fp16_overflow 0
		.amdhsa_tg_split 0
		.amdhsa_exception_fp_ieee_invalid_op 0
		.amdhsa_exception_fp_denorm_src 0
		.amdhsa_exception_fp_ieee_div_zero 0
		.amdhsa_exception_fp_ieee_overflow 0
		.amdhsa_exception_fp_ieee_underflow 0
		.amdhsa_exception_fp_ieee_inexact 0
		.amdhsa_exception_int_div_zero 0
	.end_amdhsa_kernel

amdhsa.kernels:
  - .agpr_count:     0
    .args:
      - .offset:         0
        .size:           144
        .value_kind:     by_value
    .group_segment_fixed_size: 16640
    .kernarg_segment_align: 8
    .kernarg_segment_size: 144
    .language:       OpenCL C
    .language_version:
      - 2
      - 0
    .max_flat_workgroup_size: 256
    .name:           _Z8prep_ln18PrepArgs
    .private_segment_fixed_size: 0
    .sgpr_count:     18
    .sgpr_spill_count: 0
    .symbol:         _Z8prep_ln18PrepArgs.kd
    .uniform_work_group_size: 1
    .uses_dynamic_stack: false
    .vgpr_count:     61
    .vgpr_spill_count: 0
    .wavefront_size: 64
  - .agpr_count:     0
    .args:
      - .address_space:  global
        .offset:         0
        .size:           8
        .value_kind:     global_buffer
      - .address_space:  global
        .offset:         8
        .size:           8
        .value_kind:     global_buffer
      - .address_space:  global
        .offset:         16
        .size:           8
        .value_kind:     global_buffer
      - .address_space:  global
        .offset:         24
        .size:           8
        .value_kind:     global_buffer
      - .offset:         32
        .size:           144
        .value_kind:     by_value
    .group_segment_fixed_size: 0
    .kernarg_segment_align: 8
    .kernarg_segment_size: 176
    .language:       OpenCL C
    .language_version:
      - 2
      - 0
    .max_flat_workgroup_size: 256
    .name:           _Z10attn64_fwdPKtS0_S0_Pt8PrepArgs
    .private_segment_fixed_size: 0
    .sgpr_count:     42
    .sgpr_spill_count: 0
    .symbol:         _Z10attn64_fwdPKtS0_S0_Pt8PrepArgs.kd
    .uniform_work_group_size: 1
    .uses_dynamic_stack: false
    .vgpr_count:     221
    .vgpr_spill_count: 0
    .wavefront_size: 64
  - .agpr_count:     0
    .args:
      - .address_space:  global
        .offset:         0
        .size:           8
        .value_kind:     global_buffer
      - .address_space:  global
        .offset:         8
        .size:           8
        .value_kind:     global_buffer
      - .offset:         16
        .size:           4
        .value_kind:     by_value
      - .offset:         20
        .size:           4
        .value_kind:     by_value
      - .offset:         24
        .size:           64
        .value_kind:     by_value
    .group_segment_fixed_size: 0
    .kernarg_segment_align: 8
    .kernarg_segment_size: 88
    .language:       OpenCL C
    .language_version:
      - 2
      - 0
    .max_flat_workgroup_size: 256
    .name:           _Z8gemm2b_kILi2EEvPKtS1_ii7EpiArgs
    .private_segment_fixed_size: 0
    .sgpr_count:     98
    .sgpr_spill_count: 0
    .symbol:         _Z8gemm2b_kILi2EEvPKtS1_ii7EpiArgs.kd
    .uniform_work_group_size: 1
    .uses_dynamic_stack: false
    .vgpr_count:     212
    .vgpr_spill_count: 0
    .wavefront_size: 64
  - .agpr_count:     0
    .args:
      - .address_space:  global
        .offset:         0
        .size:           8
        .value_kind:     global_buffer
      - .address_space:  global
        .offset:         8
        .size:           8
        .value_kind:     global_buffer
      - .offset:         16
        .size:           4
        .value_kind:     by_value
      - .offset:         20
        .size:           4
        .value_kind:     by_value
      - .offset:         24
        .size:           64
        .value_kind:     by_value
    .group_segment_fixed_size: 0
    .kernarg_segment_align: 8
    .kernarg_segment_size: 88
    .language:       OpenCL C
    .language_version:
      - 2
      - 0
    .max_flat_workgroup_size: 256
    .name:           _Z8gemm2b_kILi0EEvPKtS1_ii7EpiArgs
    .private_segment_fixed_size: 0
    .sgpr_count:     85
    .sgpr_spill_count: 0
    .symbol:         _Z8gemm2b_kILi0EEvPKtS1_ii7EpiArgs.kd
    .uniform_work_group_size: 1
    .uses_dynamic_stack: false
    .vgpr_count:     186
    .vgpr_spill_count: 0
    .wavefront_size: 64
  - .agpr_count:     0
    .args:
      - .address_space:  global
        .offset:         0
        .size:           8
        .value_kind:     global_buffer
      - .address_space:  global
        .offset:         8
        .size:           8
        .value_kind:     global_buffer
      - .offset:         16
        .size:           4
        .value_kind:     by_value
      - .offset:         20
        .size:           4
        .value_kind:     by_value
      - .offset:         24
        .size:           64
        .value_kind:     by_value
    .group_segment_fixed_size: 0
    .kernarg_segment_align: 8
    .kernarg_segment_size: 88
    .language:       OpenCL C
    .language_version:
      - 2
      - 0
    .max_flat_workgroup_size: 512
    .name:           _Z6gemm_kILi1ELb1ELb0ELb1ELb1ELb0EEvPKtS1_ii7EpiArgs
    .private_segment_fixed_size: 0
    .sgpr_count:     76
    .sgpr_spill_count: 0
    .symbol:         _Z6gemm_kILi1ELb1ELb0ELb1ELb1ELb0EEvPKtS1_ii7EpiArgs.kd
    .uniform_work_group_size: 1
    .uses_dynamic_stack: false
    .vgpr_count:     145
    .vgpr_spill_count: 0
    .wavefront_size: 64
  - .agpr_count:     0
    .args:
      - .address_space:  global
        .offset:         0
        .size:           8
        .value_kind:     global_buffer
      - .address_space:  global
        .offset:         8
        .size:           8
        .value_kind:     global_buffer
      - .offset:         16
        .size:           4
        .value_kind:     by_value
      - .offset:         20
        .size:           4
        .value_kind:     by_value
      - .offset:         24
        .size:           64
        .value_kind:     by_value
    .group_segment_fixed_size: 0
    .kernarg_segment_align: 8
    .kernarg_segment_size: 88
    .language:       OpenCL C
    .language_version:
      - 2
      - 0
    .max_flat_workgroup_size: 512
    .name:           _Z6gemm_kILi1ELb1ELb1ELb0ELb0ELb1EEvPKtS1_ii7EpiArgs
    .private_segment_fixed_size: 0
    .sgpr_count:     84
    .sgpr_spill_count: 0
    .symbol:         _Z6gemm_kILi1ELb1ELb1ELb0ELb0ELb1EEvPKtS1_ii7EpiArgs.kd
    .uniform_work_group_size: 1
    .uses_dynamic_stack: false
    .vgpr_count:     224
    .vgpr_spill_count: 0
    .wavefront_size: 64
